# speedup vs baseline: 1.0027x; 1.0027x over previous
.Lattn_prio_done:
.LBB2_5:
	s_add_i32 s26, s26, 2
	v_add_u32_e32 v191, s3, v187
	ds_read_b64_tr_b16 v[176:177], v191 offset:24576
	ds_read_b64_tr_b16 v[178:179], v191 offset:25088
	v_mfma_f32_32x32x16_f16 v[96:111], v[172:175], v[124:127], v[32:47]
	v_exp_f32_e32 v56, v56
	v_cvt_pk_f16_f32 v140, v64, v65
	v_exp_f32_e32 v57, v57
	v_cvt_pk_f16_f32 v141, v66, v67
	ds_read_b64_tr_b16 v[172:173], v191 offset:28672
	ds_read_b64_tr_b16 v[174:175], v191 offset:29184
	v_mfma_f32_32x32x16_f16 v[80:95], v[168:171], v[124:127], v[32:47]
	v_exp_f32_e32 v58, v58
	v_cvt_pk_f16_f32 v142, v68, v69
	v_exp_f32_e32 v59, v59
	v_cvt_pk_f16_f32 v143, v70, v71
	v_pk_add_f16 v128, v140, v141
	ds_read_b64_tr_b16 v[64:65], v191 offset:25600
	ds_read_b64_tr_b16 v[66:67], v191 offset:26112
	v_mfma_f32_32x32x16_f16 v[96:111], v[164:167], v[120:123], v[96:111]
	v_exp_f32_e32 v60, v60
	v_cvt_pk_f16_f32 v136, v72, v73
	v_exp_f32_e32 v61, v61
	v_cvt_pk_f16_f32 v137, v74, v75
	v_pk_add_f16 v129, v142, v143
	ds_read_b64_tr_b16 v[68:69], v191 offset:29696
	ds_read_b64_tr_b16 v[70:71], v191 offset:30208
	v_mfma_f32_32x32x16_f16 v[80:95], v[160:163], v[120:123], v[80:95]
	v_exp_f32_e32 v62, v62
	v_cvt_pk_f16_f32 v138, v76, v77
	v_exp_f32_e32 v63, v63
	v_cvt_pk_f16_f32 v139, v78, v79
	v_pk_add_f16 v72, v136, v137
	v_pk_add_f16 v128, v128, v129
	s_min_u32 s2, s26, 28
	s_lshl_b32 s2, s2, 13
	s_add_u32 s2, s14, s2
	s_addc_u32 s3, s15, 0
	s_add_u32 s2, s2, 0x6000
	s_addc_u32 s3, s3, 0
	s_add_i32 s4, s31, s24
	s_mov_b32 s5, m0
	s_mov_b32 m0, s4
	s_nop 0
	global_load_lds_dwordx4 v189, s[2:3]
	s_mov_b32 m0, s5
	ds_read_b64_tr_b16 v[76:77], v191 offset:26624
	ds_read_b64_tr_b16 v[78:79], v191 offset:27136
	v_mfma_f32_32x32x16_f16 v[96:111], v[156:159], v[116:119], v[96:111]
	v_pk_add_f16 v73, v138, v139
	v_cvt_pk_f16_f32 v132, v48, v49
	v_cvt_pk_f16_f32 v133, v50, v51
	ds_read_b64_tr_b16 v[48:49], v191 offset:30720
	ds_read_b64_tr_b16 v[50:51], v191 offset:31232
	v_mfma_f32_32x32x16_f16 v[80:95], v[152:155], v[116:119], v[80:95]
	v_pk_add_f16 v129, v72, v73
	v_cvt_pk_f16_f32 v134, v52, v53
	v_cvt_pk_f16_f32 v135, v54, v55
	v_pk_add_f16 v156, v132, v133
	s_add_u32 s2, s27, 0x2000
	s_addc_u32 s3, s28, 0
	s_add_i32 s4, s29, s25
	s_mov_b32 s5, m0
	s_mov_b32 m0, s4
	s_nop 0
	global_load_lds_dwordx4 v189, s[2:3]
	s_mov_b32 m0, s5
	ds_read_b64_tr_b16 v[72:73], v191 offset:27648
	ds_read_b64_tr_b16 v[74:75], v191 offset:28160
	v_mfma_f32_32x32x16_f16 v[96:111], v[148:151], v[112:115], v[96:111]
	v_pk_add_f16 v153, v128, v129
	v_cvt_pk_f16_f32 v128, v56, v57
	v_cvt_pk_f16_f32 v129, v58, v59
	v_pk_add_f16 v152, v134, v135
	ds_read_b64_tr_b16 v[52:53], v191 offset:31744
	ds_read_b64_tr_b16 v[54:55], v191 offset:32256
	v_mfma_f32_32x32x16_f16 v[80:95], v[144:147], v[112:115], v[80:95]
	v_pk_add_f16 v56, v128, v129
	v_pk_add_f16 v57, v156, v152
	v_cvt_pk_f16_f32 v130, v60, v61
	v_cvt_pk_f16_f32 v131, v62, v63
	s_andn2_b64 vcc, exec, s[18:19]
	v_pk_add_f16 v57, v153, v57
	v_pk_add_f16 v58, v130, v131
	s_cbranch_vccnz .LBB2_7
	v_pk_add_f16 v59, v56, v58
	v_max3_f32 v61, v96, v97, v80
	v_max3_f32 v62, v98, v99, v81
	s_mov_b64 s[8:9], 0
	v_pk_add_f16 v59, v57, v59
	s_nop 0
	v_cvt_f32_f16_e32 v60, v59
	v_cvt_f32_f16_sdwa v59, v59 dst_sel:DWORD dst_unused:UNUSED_PAD src0_sel:WORD_1
	v_add_f32_e32 v59, v59, v60
	v_add_f32_e32 v188, v188, v59
	v_max3_f32 v59, v61, v82, v83
	v_max3_f32 v60, v62, v102, v103
	s_nop 0
	v_max3_f32 v59, v59, v100, v101
	v_max3_f32 v60, v60, v86, v87
	s_nop 0
	v_max3_f32 v59, v59, v84, v85
	v_max3_f32 v60, v60, v106, v107
	s_nop 0
	v_max3_f32 v59, v59, v104, v105
	v_max3_f32 v60, v60, v90, v91
	s_nop 0
	v_max3_f32 v59, v59, v88, v89
	v_max3_f32 v60, v60, v110, v111
	s_nop 0
	v_max3_f32 v59, v59, v108, v109
	v_max3_f32 v60, v60, v94, v95
	s_nop 0
	v_max3_f32 v59, v59, v92, v93
	s_nop 0
	v_max_f32 v59, v59, v60
	s_nop 0
	v_mov_b32_e32 v60, v59
	s_nop 1
	v_permlane32_swap_b32_e32 v59, v60
	v_max_f32 v59, v59, v60
	s_nop 0
	v_cmp_lt_f32_e32 vcc, s30, v59
	s_cbranch_vccnz .LBB2_19

.LBB2_11:
	s_add_i32 s33, s29, 0x2000
	s_cmpk_lg_i32 s29, 0x4000
	s_cselect_b32 s33, s33, 0
	v_add_u32_e32 v191, s31, v187
	ds_read_b64_tr_b16 v[148:149], v191 offset:24576
	ds_read_b64_tr_b16 v[150:151], v191 offset:25088
	s_waitcnt lgkmcnt(9)
	v_mfma_f32_32x32x16_f16 v[64:79], v[56:59], v[124:127], v[32:47]
	v_exp_f32_e32 v88, v88
	v_cvt_pk_f16_f32 v140, v96, v97
	v_exp_f32_e32 v89, v89
	v_cvt_pk_f16_f32 v141, v98, v99
	ds_read_b64_tr_b16 v[144:145], v191 offset:28672
	ds_read_b64_tr_b16 v[146:147], v191 offset:29184
	s_waitcnt lgkmcnt(10)
	v_mfma_f32_32x32x16_f16 v[48:63], v[176:179], v[124:127], v[32:47]
	v_exp_f32_e32 v90, v90
	v_cvt_pk_f16_f32 v142, v100, v101
	v_exp_f32_e32 v91, v91
	v_cvt_pk_f16_f32 v143, v102, v103
	v_pk_add_f16 v128, v140, v141
	ds_read_b64_tr_b16 v[96:97], v191 offset:25600
	ds_read_b64_tr_b16 v[98:99], v191 offset:26112
	s_waitcnt lgkmcnt(11)
	v_mfma_f32_32x32x16_f16 v[64:79], v[172:175], v[120:123], v[64:79]
	v_exp_f32_e32 v92, v92
	v_cvt_pk_f16_f32 v136, v104, v105
	v_exp_f32_e32 v93, v93
	v_cvt_pk_f16_f32 v137, v106, v107
	v_pk_add_f16 v129, v142, v143
	ds_read_b64_tr_b16 v[100:101], v191 offset:29696
	ds_read_b64_tr_b16 v[102:103], v191 offset:30208
	s_waitcnt lgkmcnt(12)
	v_mfma_f32_32x32x16_f16 v[48:63], v[168:171], v[120:123], v[48:63]
	v_exp_f32_e32 v94, v94
	v_cvt_pk_f16_f32 v138, v108, v109
	v_exp_f32_e32 v95, v95
	v_cvt_pk_f16_f32 v139, v110, v111
	v_pk_add_f16 v128, v128, v129
	v_pk_add_f16 v172, v136, v137
	s_min_u32 s31, s26, 27
	s_lshl_b32 s31, s31, 13
	s_add_u32 s31, s14, s31
	s_addc_u32 s35, s15, 0
	s_add_u32 s34, s31, 0x8000
	s_addc_u32 s35, s35, 0
	s_add_i32 s31, s29, s24
	s_mov_b32 s36, m0
	s_mov_b32 m0, s31
	s_nop 0
	global_load_lds_dwordx4 v189, s[34:35]
	s_mov_b32 m0, s36
	ds_read_b64_tr_b16 v[104:105], v191 offset:26624
	ds_read_b64_tr_b16 v[106:107], v191 offset:27136
	s_waitcnt lgkmcnt(13)
	v_mfma_f32_32x32x16_f16 v[64:79], v[164:167], v[116:119], v[64:79]
	v_pk_add_f16 v108, v138, v139
	v_cvt_pk_f16_f32 v132, v80, v81
	v_cvt_pk_f16_f32 v133, v82, v83
	ds_read_b64_tr_b16 v[80:81], v191 offset:30720
	ds_read_b64_tr_b16 v[82:83], v191 offset:31232
	s_waitcnt lgkmcnt(14)
	v_mfma_f32_32x32x16_f16 v[48:63], v[160:163], v[116:119], v[48:63]
	v_pk_add_f16 v129, v172, v108
	v_cvt_pk_f16_f32 v134, v84, v85
	v_cvt_pk_f16_f32 v135, v86, v87
	v_pk_add_f16 v164, v132, v133
	s_add_u32 s34, s27, 0x4000
	s_addc_u32 s35, s28, 0
	s_add_i32 s31, s33, s25
	s_mov_b32 s36, m0
	s_mov_b32 m0, s31
	s_nop 0
	global_load_lds_dwordx4 v189, s[34:35]
	s_mov_b32 m0, s36
	ds_read_b64_tr_b16 v[108:109], v191 offset:27648
	ds_read_b64_tr_b16 v[110:111], v191 offset:28160
	s_waitcnt lgkmcnt(14)
	v_mfma_f32_32x32x16_f16 v[64:79], v[156:159], v[112:115], v[64:79]
	v_pk_add_f16 v161, v128, v129
	v_cvt_pk_f16_f32 v128, v88, v89
	v_cvt_pk_f16_f32 v129, v90, v91
	v_pk_add_f16 v160, v134, v135
	ds_read_b64_tr_b16 v[84:85], v191 offset:31744
	ds_read_b64_tr_b16 v[86:87], v191 offset:32256
	v_mfma_f32_32x32x16_f16 v[48:63], v[152:155], v[112:115], v[48:63]
	v_pk_add_f16 v88, v128, v129
	v_pk_add_f16 v89, v164, v160
	v_cvt_pk_f16_f32 v130, v92, v93
	v_cvt_pk_f16_f32 v131, v94, v95
	s_and_b64 vcc, exec, s[16:17]
	v_pk_add_f16 v89, v161, v89
	v_pk_add_f16 v90, v130, v131
	s_cbranch_vccnz .LBB2_13
	v_pk_add_f16 v91, v88, v90
	v_max3_f32 v93, v64, v65, v48
	v_max3_f32 v94, v66, v67, v49
	s_mov_b64 s[8:9], 0
	v_pk_add_f16 v91, v89, v91
	s_nop 0
	v_cvt_f32_f16_e32 v92, v91
	v_cvt_f32_f16_sdwa v91, v91 dst_sel:DWORD dst_unused:UNUSED_PAD src0_sel:WORD_1
	v_add_f32_e32 v91, v91, v92
	v_add_f32_e32 v188, v188, v91
	v_max3_f32 v91, v93, v50, v51
	v_max3_f32 v92, v94, v70, v71
	s_nop 0
	v_max3_f32 v91, v91, v68, v69
	v_max3_f32 v92, v92, v54, v55
	s_nop 0
	v_max3_f32 v91, v91, v52, v53
	v_max3_f32 v92, v92, v74, v75
	s_nop 0
	v_max3_f32 v91, v91, v72, v73
	v_max3_f32 v92, v92, v58, v59
	s_nop 0
	v_max3_f32 v91, v91, v56, v57
	v_max3_f32 v92, v92, v78, v79
	s_nop 0
	v_max3_f32 v91, v91, v76, v77
	v_max3_f32 v92, v92, v62, v63
	s_nop 0
	v_max3_f32 v91, v91, v60, v61
	s_nop 0
	v_max_f32 v91, v91, v92
	s_nop 0
	v_mov_b32_e32 v92, v91
	s_nop 1
	v_permlane32_swap_b32_e32 v91, v92
	v_max_f32 v91, v91, v92
	s_nop 0
	v_cmp_lt_f32_e32 vcc, s30, v91
	s_cbranch_vccnz .LBB2_22
